# down-projection tile body as 32-step software pipeline (ring of 4 LDS half-slabs, rolling B prefetch, deferred epilogue under next MFMAs) plus nt hint on its Y8 stores
# baseline (speedup 1.0000x reference)
.Ldown_mid:
	s_waitcnt vmcnt(2) lgkmcnt(0)
	s_barrier
	s_add_i32 m0, s30, 0xc000
	s_nop 0
	global_load_lds_dwordx4 v176, s[16:17]
	s_add_i32 m0, s30, 0xe000
	s_nop 0
	global_load_lds_dwordx4 v64, s[16:17]
	s_add_u32 s16, s16, 0x4000
	s_addc_u32 s17, s17, 0
	v_mfma_f32_16x16x32_bf16 v[178:181], v[112:115], v[0:3], 0
	v_mfma_f32_16x16x32_bf16 v[182:185], v[116:119], v[0:3], 0
	ds_read_b128 v[160:163], v100 offset:16384
	ds_read_b128 v[164:167], v100 offset:24576
	v_mfma_f32_16x16x32_bf16 v[186:189], v[112:115], v[32:35], 0
	v_mfma_f32_16x16x32_bf16 v[190:193], v[116:119], v[32:35], 0
	ds_read_b128 v[168:171], v101 offset:16384
	ds_read_b128 v[172:175], v101 offset:24576
	v_max3_f32 v77, |v194|, |v195|, |v196|
	v_max3_f32 v84, |v202|, |v203|, |v204|
	v_mfma_f32_16x16x32_bf16 v[178:181], v[120:123], v[4:7], v[178:181]
	v_max3_f32 v78, |v197|, |v198|, |v199|
	v_max3_f32 v85, |v205|, |v206|, |v207|
	v_mfma_f32_16x16x32_bf16 v[182:185], v[124:127], v[4:7], v[182:185]
	v_max3_f32 v77, |v200|, |v201|, v77
	v_max3_f32 v84, |v208|, |v209|, v84
	v_mfma_f32_16x16x32_bf16 v[186:189], v[120:123], v[36:39], v[186:189]
	v_max_f32_e32 v77, v77, v78
	v_max_f32_e32 v84, v84, v85
	v_mfma_f32_16x16x32_bf16 v[190:193], v[124:127], v[36:39], v[190:193]
	ds_read_b128 v[112:115], v94 offset:16384
	ds_read_b128 v[116:119], v94 offset:24576
	v_mul_f32_e32 v77, 0x3c010204, v77
	v_mul_f32_e32 v84, 0x3c010204, v84
	v_mfma_f32_16x16x32_bf16 v[178:181], v[128:131], v[8:11], v[178:181]
	v_lshrrev_b32_e32 v79, 23, v77
	v_lshrrev_b32_e32 v110, 23, v84
	v_mfma_f32_16x16x32_bf16 v[182:185], v[132:135], v[8:11], v[182:185]
	v_and_b32_e32 v77, 0x7f800000, v77
	v_and_b32_e32 v84, 0x7f800000, v84
	v_mfma_f32_16x16x32_bf16 v[186:189], v[128:131], v[40:43], v[186:189]
	v_sub_u32_e32 v77, 0x7e800000, v77
	v_sub_u32_e32 v84, 0x7e800000, v84
	v_mfma_f32_16x16x32_bf16 v[190:193], v[132:135], v[40:43], v[190:193]
	ds_read_b128 v[120:123], v95 offset:16384
	ds_read_b128 v[124:127], v95 offset:24576
	v_fmaak_f32 v78, v194, v77, 0x43000000
	v_fmaak_f32 v85, v202, v84, 0x43000000
	v_mfma_f32_16x16x32_bf16 v[178:181], v[136:139], v[12:15], v[178:181]
	v_cvt_pk_u8_f32 v80, v78, 0, 0
	v_cvt_pk_u8_f32 v82, v85, 0, 0
	v_mfma_f32_16x16x32_bf16 v[182:185], v[140:143], v[12:15], v[182:185]
	v_fmaak_f32 v78, v195, v77, 0x43000000
	v_fmaak_f32 v85, v203, v84, 0x43000000
	v_mfma_f32_16x16x32_bf16 v[186:189], v[136:139], v[44:47], v[186:189]
	v_cvt_pk_u8_f32 v80, v78, 1, v80
	v_cvt_pk_u8_f32 v82, v85, 1, v82
	v_mfma_f32_16x16x32_bf16 v[190:193], v[140:143], v[44:47], v[190:193]
	ds_read_b128 v[128:131], v96 offset:16384
	ds_read_b128 v[132:135], v96 offset:24576
	v_fmaak_f32 v78, v196, v77, 0x43000000
	v_fmaak_f32 v85, v204, v84, 0x43000000
	v_mfma_f32_16x16x32_bf16 v[178:181], v[144:147], v[16:19], v[178:181]
	v_cvt_pk_u8_f32 v80, v78, 2, v80
	v_cvt_pk_u8_f32 v82, v85, 2, v82
	v_mfma_f32_16x16x32_bf16 v[182:185], v[148:151], v[16:19], v[182:185]
	v_fmaak_f32 v78, v197, v77, 0x43000000
	v_fmaak_f32 v85, v205, v84, 0x43000000
	v_mfma_f32_16x16x32_bf16 v[186:189], v[144:147], v[48:51], v[186:189]
	v_cvt_pk_u8_f32 v80, v78, 3, v80
	v_cvt_pk_u8_f32 v82, v85, 3, v82
	v_mfma_f32_16x16x32_bf16 v[190:193], v[148:151], v[48:51], v[190:193]
	ds_read_b128 v[136:139], v97 offset:16384
	ds_read_b128 v[140:143], v97 offset:24576
	v_fmaak_f32 v78, v198, v77, 0x43000000
	v_fmaak_f32 v85, v206, v84, 0x43000000
	v_mfma_f32_16x16x32_bf16 v[178:181], v[152:155], v[20:23], v[178:181]
	v_cvt_pk_u8_f32 v81, v78, 0, 0
	v_cvt_pk_u8_f32 v83, v85, 0, 0
	v_mfma_f32_16x16x32_bf16 v[182:185], v[156:159], v[20:23], v[182:185]
	v_fmaak_f32 v78, v199, v77, 0x43000000
	v_fmaak_f32 v85, v207, v84, 0x43000000
	v_mfma_f32_16x16x32_bf16 v[186:189], v[152:155], v[52:55], v[186:189]
	v_cvt_pk_u8_f32 v81, v78, 1, v81
	v_cvt_pk_u8_f32 v83, v85, 1, v83
	v_mfma_f32_16x16x32_bf16 v[190:193], v[156:159], v[52:55], v[190:193]
	ds_read_b128 v[144:147], v98 offset:16384
	ds_read_b128 v[148:151], v98 offset:24576
	v_fmaak_f32 v78, v200, v77, 0x43000000
	v_fmaak_f32 v85, v208, v84, 0x43000000
	v_mfma_f32_16x16x32_bf16 v[178:181], v[210:213], v[24:27], v[178:181]
	v_cvt_pk_u8_f32 v81, v78, 2, v81
	v_cvt_pk_u8_f32 v83, v85, 2, v83
	v_mfma_f32_16x16x32_bf16 v[182:185], v[214:217], v[24:27], v[182:185]
	v_fmaak_f32 v78, v201, v77, 0x43000000
	v_fmaak_f32 v85, v209, v84, 0x43000000
	v_mfma_f32_16x16x32_bf16 v[186:189], v[210:213], v[56:59], v[186:189]
	v_cvt_pk_u8_f32 v81, v78, 3, v81
	v_cvt_pk_u8_f32 v83, v85, 3, v83
	v_mfma_f32_16x16x32_bf16 v[190:193], v[214:217], v[56:59], v[190:193]
	ds_read_b128 v[152:155], v99 offset:16384
	ds_read_b128 v[156:159], v99 offset:24576
	v_add_u16_e32 v79, 1, v79
	v_add_u16_e32 v110, 1, v110
	v_mfma_f32_16x16x32_bf16 v[178:181], v[236:239], v[28:31], v[178:181]
	ds_write_b8 v106, v79 offset:140
	ds_write_b8 v106, v110 offset:2700
	v_mfma_f32_16x16x32_bf16 v[182:185], v[240:243], v[28:31], v[182:185]
	ds_write2st64_b64 v109, v[80:81], v[82:83] offset1:5
	v_mfma_f32_16x16x32_bf16 v[186:189], v[236:239], v[60:63], v[186:189]
	v_mfma_f32_16x16x32_bf16 v[190:193], v[240:243], v[60:63], v[190:193]
	s_waitcnt lgkmcnt(0)
	ds_read_b128 v[194:197], v103
	ds_read_b128 v[198:201], v103 offset:1280
	ds_read_b128 v[202:205], v103 offset:2560
	ds_read_b128 v[206:209], v103 offset:3840
	ds_read_b128 v[244:247], v104 offset:128
	s_waitcnt vmcnt(2) lgkmcnt(0)
	s_barrier
	global_store_dwordx4 v72, v[194:197], s[10:11] nt
	global_store_dwordx4 v73, v[198:201], s[10:11] nt
	global_store_dwordx4 v74, v[202:205], s[10:11] nt
	global_store_dwordx4 v75, v[206:209], s[10:11] nt
	s_and_saveexec_b64 s[8:9], s[2:3]
	global_store_dwordx4 v76, v[244:247], s[10:11] nt
	s_or_b64 exec, exec, s[8:9]
	v_add_u32_e32 v72, 0x80, v72
	v_add_u32_e32 v73, 0x80, v73
	v_add_u32_e32 v74, 0x80, v74
	v_add_u32_e32 v75, 0x80, v75
	v_add_u32_e32 v76, 16, v76
	s_mov_b32 m0, s30
	s_nop 0
	global_load_lds_dwordx4 v176, s[16:17]
	s_add_i32 m0, s30, 0x2000
	s_nop 0
	global_load_lds_dwordx4 v64, s[16:17]
	s_add_u32 s16, s16, 0x4000
	s_addc_u32 s17, s17, 0
	v_mfma_f32_16x16x32_bf16 v[194:197], v[112:115], v[0:3], 0
	v_mfma_f32_16x16x32_bf16 v[198:201], v[116:119], v[0:3], 0
	ds_read_b128 v[210:213], v100 offset:32768
	ds_read_b128 v[214:217], v100 offset:40960
	v_mfma_f32_16x16x32_bf16 v[202:205], v[112:115], v[32:35], 0
	v_mfma_f32_16x16x32_bf16 v[206:209], v[116:119], v[32:35], 0
	ds_read_b128 v[236:239], v101 offset:32768
	ds_read_b128 v[240:243], v101 offset:40960
	v_max3_f32 v77, |v178|, |v179|, |v180|
	v_max3_f32 v84, |v186|, |v187|, |v188|
	v_mfma_f32_16x16x32_bf16 v[194:197], v[120:123], v[4:7], v[194:197]
	v_max3_f32 v78, |v181|, |v182|, |v183|
	v_max3_f32 v85, |v189|, |v190|, |v191|
	v_mfma_f32_16x16x32_bf16 v[198:201], v[124:127], v[4:7], v[198:201]
	v_max3_f32 v77, |v184|, |v185|, v77
	v_max3_f32 v84, |v192|, |v193|, v84
	v_mfma_f32_16x16x32_bf16 v[202:205], v[120:123], v[36:39], v[202:205]
	v_max_f32_e32 v77, v77, v78
	v_max_f32_e32 v84, v84, v85
	v_mfma_f32_16x16x32_bf16 v[206:209], v[124:127], v[36:39], v[206:209]
	ds_read_b128 v[112:115], v94 offset:32768
	ds_read_b128 v[116:119], v94 offset:40960
	v_mul_f32_e32 v77, 0x3c010204, v77
	v_mul_f32_e32 v84, 0x3c010204, v84
	v_mfma_f32_16x16x32_bf16 v[194:197], v[128:131], v[8:11], v[194:197]
	v_lshrrev_b32_e32 v79, 23, v77
	v_lshrrev_b32_e32 v110, 23, v84
	v_mfma_f32_16x16x32_bf16 v[198:201], v[132:135], v[8:11], v[198:201]
	v_and_b32_e32 v77, 0x7f800000, v77
	v_and_b32_e32 v84, 0x7f800000, v84
	v_mfma_f32_16x16x32_bf16 v[202:205], v[128:131], v[40:43], v[202:205]
	v_sub_u32_e32 v77, 0x7e800000, v77
	v_sub_u32_e32 v84, 0x7e800000, v84
	v_mfma_f32_16x16x32_bf16 v[206:209], v[132:135], v[40:43], v[206:209]
	ds_read_b128 v[120:123], v95 offset:32768
	ds_read_b128 v[124:127], v95 offset:40960
	v_fmaak_f32 v78, v178, v77, 0x43000000
	v_fmaak_f32 v85, v186, v84, 0x43000000
	v_mfma_f32_16x16x32_bf16 v[194:197], v[136:139], v[12:15], v[194:197]
	v_cvt_pk_u8_f32 v80, v78, 0, 0
	v_cvt_pk_u8_f32 v82, v85, 0, 0
	v_mfma_f32_16x16x32_bf16 v[198:201], v[140:143], v[12:15], v[198:201]
	v_fmaak_f32 v78, v179, v77, 0x43000000
	v_fmaak_f32 v85, v187, v84, 0x43000000
	v_mfma_f32_16x16x32_bf16 v[202:205], v[136:139], v[44:47], v[202:205]
	v_cvt_pk_u8_f32 v80, v78, 1, v80
	v_cvt_pk_u8_f32 v82, v85, 1, v82
	v_mfma_f32_16x16x32_bf16 v[206:209], v[140:143], v[44:47], v[206:209]
	ds_read_b128 v[128:131], v96 offset:32768
	ds_read_b128 v[132:135], v96 offset:40960
	v_fmaak_f32 v78, v180, v77, 0x43000000
	v_fmaak_f32 v85, v188, v84, 0x43000000
	v_mfma_f32_16x16x32_bf16 v[194:197], v[144:147], v[16:19], v[194:197]
	v_cvt_pk_u8_f32 v80, v78, 2, v80
	v_cvt_pk_u8_f32 v82, v85, 2, v82
	v_mfma_f32_16x16x32_bf16 v[198:201], v[148:151], v[16:19], v[198:201]
	v_fmaak_f32 v78, v181, v77, 0x43000000
	v_fmaak_f32 v85, v189, v84, 0x43000000
	v_mfma_f32_16x16x32_bf16 v[202:205], v[144:147], v[48:51], v[202:205]
	v_cvt_pk_u8_f32 v80, v78, 3, v80
	v_cvt_pk_u8_f32 v82, v85, 3, v82
	v_mfma_f32_16x16x32_bf16 v[206:209], v[148:151], v[48:51], v[206:209]
	ds_read_b128 v[136:139], v97 offset:32768
	ds_read_b128 v[140:143], v97 offset:40960
	v_fmaak_f32 v78, v182, v77, 0x43000000
	v_fmaak_f32 v85, v190, v84, 0x43000000
	v_mfma_f32_16x16x32_bf16 v[194:197], v[152:155], v[20:23], v[194:197]
	v_cvt_pk_u8_f32 v81, v78, 0, 0
	v_cvt_pk_u8_f32 v83, v85, 0, 0
	v_mfma_f32_16x16x32_bf16 v[198:201], v[156:159], v[20:23], v[198:201]
	v_fmaak_f32 v78, v183, v77, 0x43000000
	v_fmaak_f32 v85, v191, v84, 0x43000000
	v_mfma_f32_16x16x32_bf16 v[202:205], v[152:155], v[52:55], v[202:205]
	v_cvt_pk_u8_f32 v81, v78, 1, v81
	v_cvt_pk_u8_f32 v83, v85, 1, v83
	v_mfma_f32_16x16x32_bf16 v[206:209], v[156:159], v[52:55], v[206:209]
	ds_read_b128 v[144:147], v98 offset:32768
	ds_read_b128 v[148:151], v98 offset:40960
	v_fmaak_f32 v78, v184, v77, 0x43000000
	v_fmaak_f32 v85, v192, v84, 0x43000000
	v_mfma_f32_16x16x32_bf16 v[194:197], v[160:163], v[24:27], v[194:197]
	v_cvt_pk_u8_f32 v81, v78, 2, v81
	v_cvt_pk_u8_f32 v83, v85, 2, v83
	v_mfma_f32_16x16x32_bf16 v[198:201], v[164:167], v[24:27], v[198:201]
	v_fmaak_f32 v78, v185, v77, 0x43000000
	v_fmaak_f32 v85, v193, v84, 0x43000000
	v_mfma_f32_16x16x32_bf16 v[202:205], v[160:163], v[56:59], v[202:205]
	v_cvt_pk_u8_f32 v81, v78, 3, v81
	v_cvt_pk_u8_f32 v83, v85, 3, v83
	v_mfma_f32_16x16x32_bf16 v[206:209], v[164:167], v[56:59], v[206:209]
	ds_read_b128 v[152:155], v99 offset:32768
	ds_read_b128 v[156:159], v99 offset:40960
	v_add_u16_e32 v79, 1, v79
	v_add_u16_e32 v110, 1, v110
	v_mfma_f32_16x16x32_bf16 v[194:197], v[168:171], v[28:31], v[194:197]
	ds_write_b8 v106, v79 offset:128
	ds_write_b8 v106, v110 offset:2688
	v_mfma_f32_16x16x32_bf16 v[198:201], v[172:175], v[28:31], v[198:201]
	ds_write2st64_b64 v102, v[80:81], v[82:83] offset1:5
	v_mfma_f32_16x16x32_bf16 v[202:205], v[168:171], v[60:63], v[202:205]
	v_mfma_f32_16x16x32_bf16 v[206:209], v[172:175], v[60:63], v[206:209]
	s_waitcnt vmcnt(7) lgkmcnt(0)
	s_barrier
	s_add_i32 m0, s30, 0x4000
	s_nop 0
	global_load_lds_dwordx4 v176, s[16:17]
	s_add_i32 m0, s30, 0x6000
	s_nop 0
	global_load_lds_dwordx4 v64, s[16:17]
	s_add_u32 s16, s16, 0x4000
	s_addc_u32 s17, s17, 0
	v_mfma_f32_16x16x32_bf16 v[178:181], v[112:115], v[0:3], 0
	v_mfma_f32_16x16x32_bf16 v[182:185], v[116:119], v[0:3], 0
	ds_read_b128 v[160:163], v100 offset:49152
	ds_read_b128 v[164:167], v100 offset:57344
	v_mfma_f32_16x16x32_bf16 v[186:189], v[112:115], v[32:35], 0
	v_mfma_f32_16x16x32_bf16 v[190:193], v[116:119], v[32:35], 0
	ds_read_b128 v[168:171], v101 offset:49152
	ds_read_b128 v[172:175], v101 offset:57344
	v_max3_f32 v77, |v194|, |v195|, |v196|
	v_max3_f32 v84, |v202|, |v203|, |v204|
	v_mfma_f32_16x16x32_bf16 v[178:181], v[120:123], v[4:7], v[178:181]
	v_max3_f32 v78, |v197|, |v198|, |v199|
	v_max3_f32 v85, |v205|, |v206|, |v207|
	v_mfma_f32_16x16x32_bf16 v[182:185], v[124:127], v[4:7], v[182:185]
	v_max3_f32 v77, |v200|, |v201|, v77
	v_max3_f32 v84, |v208|, |v209|, v84
	v_mfma_f32_16x16x32_bf16 v[186:189], v[120:123], v[36:39], v[186:189]
	v_max_f32_e32 v77, v77, v78
	v_max_f32_e32 v84, v84, v85
	v_mfma_f32_16x16x32_bf16 v[190:193], v[124:127], v[36:39], v[190:193]
	ds_read_b128 v[112:115], v94 offset:49152
	ds_read_b128 v[116:119], v94 offset:57344
	v_mul_f32_e32 v77, 0x3c010204, v77
	v_mul_f32_e32 v84, 0x3c010204, v84
	v_mfma_f32_16x16x32_bf16 v[178:181], v[128:131], v[8:11], v[178:181]
	v_lshrrev_b32_e32 v79, 23, v77
	v_lshrrev_b32_e32 v110, 23, v84
	v_mfma_f32_16x16x32_bf16 v[182:185], v[132:135], v[8:11], v[182:185]
	v_and_b32_e32 v77, 0x7f800000, v77
	v_and_b32_e32 v84, 0x7f800000, v84
	v_mfma_f32_16x16x32_bf16 v[186:189], v[128:131], v[40:43], v[186:189]
	v_sub_u32_e32 v77, 0x7e800000, v77
	v_sub_u32_e32 v84, 0x7e800000, v84
	v_mfma_f32_16x16x32_bf16 v[190:193], v[132:135], v[40:43], v[190:193]
	ds_read_b128 v[120:123], v95 offset:49152
	ds_read_b128 v[124:127], v95 offset:57344
	v_fmaak_f32 v78, v194, v77, 0x43000000
	v_fmaak_f32 v85, v202, v84, 0x43000000
	v_mfma_f32_16x16x32_bf16 v[178:181], v[136:139], v[12:15], v[178:181]
	v_cvt_pk_u8_f32 v80, v78, 0, 0
	v_cvt_pk_u8_f32 v82, v85, 0, 0
	v_mfma_f32_16x16x32_bf16 v[182:185], v[140:143], v[12:15], v[182:185]
	v_fmaak_f32 v78, v195, v77, 0x43000000
	v_fmaak_f32 v85, v203, v84, 0x43000000
	v_mfma_f32_16x16x32_bf16 v[186:189], v[136:139], v[44:47], v[186:189]
	v_cvt_pk_u8_f32 v80, v78, 1, v80
	v_cvt_pk_u8_f32 v82, v85, 1, v82
	v_mfma_f32_16x16x32_bf16 v[190:193], v[140:143], v[44:47], v[190:193]
	ds_read_b128 v[128:131], v96 offset:49152
	ds_read_b128 v[132:135], v96 offset:57344
	v_fmaak_f32 v78, v196, v77, 0x43000000
	v_fmaak_f32 v85, v204, v84, 0x43000000
	v_mfma_f32_16x16x32_bf16 v[178:181], v[144:147], v[16:19], v[178:181]
	v_cvt_pk_u8_f32 v80, v78, 2, v80
	v_cvt_pk_u8_f32 v82, v85, 2, v82
	v_mfma_f32_16x16x32_bf16 v[182:185], v[148:151], v[16:19], v[182:185]
	v_fmaak_f32 v78, v197, v77, 0x43000000
	v_fmaak_f32 v85, v205, v84, 0x43000000
	v_mfma_f32_16x16x32_bf16 v[186:189], v[144:147], v[48:51], v[186:189]
	v_cvt_pk_u8_f32 v80, v78, 3, v80
	v_cvt_pk_u8_f32 v82, v85, 3, v82
	v_mfma_f32_16x16x32_bf16 v[190:193], v[148:151], v[48:51], v[190:193]
	ds_read_b128 v[136:139], v97 offset:49152
	ds_read_b128 v[140:143], v97 offset:57344
	v_fmaak_f32 v78, v198, v77, 0x43000000
	v_fmaak_f32 v85, v206, v84, 0x43000000
	v_mfma_f32_16x16x32_bf16 v[178:181], v[152:155], v[20:23], v[178:181]
	v_cvt_pk_u8_f32 v81, v78, 0, 0
	v_cvt_pk_u8_f32 v83, v85, 0, 0
	v_mfma_f32_16x16x32_bf16 v[182:185], v[156:159], v[20:23], v[182:185]
	v_fmaak_f32 v78, v199, v77, 0x43000000
	v_fmaak_f32 v85, v207, v84, 0x43000000
	v_mfma_f32_16x16x32_bf16 v[186:189], v[152:155], v[52:55], v[186:189]
	v_cvt_pk_u8_f32 v81, v78, 1, v81
	v_cvt_pk_u8_f32 v83, v85, 1, v83
	v_mfma_f32_16x16x32_bf16 v[190:193], v[156:159], v[52:55], v[190:193]
	ds_read_b128 v[144:147], v98 offset:49152
	ds_read_b128 v[148:151], v98 offset:57344
	v_fmaak_f32 v78, v200, v77, 0x43000000
	v_fmaak_f32 v85, v208, v84, 0x43000000
	v_mfma_f32_16x16x32_bf16 v[178:181], v[210:213], v[24:27], v[178:181]
	v_cvt_pk_u8_f32 v81, v78, 2, v81
	v_cvt_pk_u8_f32 v83, v85, 2, v83
	v_mfma_f32_16x16x32_bf16 v[182:185], v[214:217], v[24:27], v[182:185]
	v_fmaak_f32 v78, v201, v77, 0x43000000
	v_fmaak_f32 v85, v209, v84, 0x43000000
	v_mfma_f32_16x16x32_bf16 v[186:189], v[210:213], v[56:59], v[186:189]
	v_cvt_pk_u8_f32 v81, v78, 3, v81
	v_cvt_pk_u8_f32 v83, v85, 3, v83
	v_mfma_f32_16x16x32_bf16 v[190:193], v[214:217], v[56:59], v[190:193]
	ds_read_b128 v[152:155], v99 offset:49152
	ds_read_b128 v[156:159], v99 offset:57344
	v_add_u16_e32 v79, 1, v79
	v_add_u16_e32 v110, 1, v110
	v_mfma_f32_16x16x32_bf16 v[178:181], v[236:239], v[28:31], v[178:181]
	ds_write_b8 v106, v79 offset:132
	ds_write_b8 v106, v110 offset:2692
	v_mfma_f32_16x16x32_bf16 v[182:185], v[240:243], v[28:31], v[182:185]
	ds_write2st64_b64 v107, v[80:81], v[82:83] offset1:5
	v_mfma_f32_16x16x32_bf16 v[186:189], v[236:239], v[60:63], v[186:189]
	v_mfma_f32_16x16x32_bf16 v[190:193], v[240:243], v[60:63], v[190:193]
	s_waitcnt vmcnt(2) lgkmcnt(0)
	s_barrier
; DI void phase_edown3(const Ctx& c, int layer) {
;     ...
;         D2_BODY(0, 0, 0); D2_BODY(1, 1, 0);
; #pragma unroll 1
;         for (int J = 2; J < 16; J += 2) { D2_BODY(0, J, 5); D2_BODY(1, J + 1, 0); }
	s_add_i32 m0, s30, 0x8000
	s_nop 0
	global_load_lds_dwordx4 v176, s[16:17]
	s_add_i32 m0, s30, 0xa000
	s_nop 0
	global_load_lds_dwordx4 v64, s[16:17]
	s_add_u32 s16, s16, 0x4000
	s_addc_u32 s17, s17, 0
	v_mfma_f32_16x16x32_bf16 v[194:197], v[112:115], v[0:3], 0
	v_mfma_f32_16x16x32_bf16 v[198:201], v[116:119], v[0:3], 0
	ds_read_b128 v[210:213], v100
	ds_read_b128 v[214:217], v100 offset:8192
	v_mfma_f32_16x16x32_bf16 v[202:205], v[112:115], v[32:35], 0
	v_mfma_f32_16x16x32_bf16 v[206:209], v[116:119], v[32:35], 0
	ds_read_b128 v[236:239], v101
	ds_read_b128 v[240:243], v101 offset:8192
	v_max3_f32 v77, |v178|, |v179|, |v180|
	v_max3_f32 v84, |v186|, |v187|, |v188|
	v_mfma_f32_16x16x32_bf16 v[194:197], v[120:123], v[4:7], v[194:197]
	v_max3_f32 v78, |v181|, |v182|, |v183|
	v_max3_f32 v85, |v189|, |v190|, |v191|
	v_mfma_f32_16x16x32_bf16 v[198:201], v[124:127], v[4:7], v[198:201]
	v_max3_f32 v77, |v184|, |v185|, v77
	v_max3_f32 v84, |v192|, |v193|, v84
	v_mfma_f32_16x16x32_bf16 v[202:205], v[120:123], v[36:39], v[202:205]
	v_max_f32_e32 v77, v77, v78
	v_max_f32_e32 v84, v84, v85
	v_mfma_f32_16x16x32_bf16 v[206:209], v[124:127], v[36:39], v[206:209]
	ds_read_b128 v[112:115], v94
	ds_read_b128 v[116:119], v94 offset:8192
	v_mul_f32_e32 v77, 0x3c010204, v77
	v_mul_f32_e32 v84, 0x3c010204, v84
	v_mfma_f32_16x16x32_bf16 v[194:197], v[128:131], v[8:11], v[194:197]
	v_lshrrev_b32_e32 v79, 23, v77
	v_lshrrev_b32_e32 v110, 23, v84
	v_mfma_f32_16x16x32_bf16 v[198:201], v[132:135], v[8:11], v[198:201]
	v_and_b32_e32 v77, 0x7f800000, v77
	v_and_b32_e32 v84, 0x7f800000, v84
	v_mfma_f32_16x16x32_bf16 v[202:205], v[128:131], v[40:43], v[202:205]
	v_sub_u32_e32 v77, 0x7e800000, v77
	v_sub_u32_e32 v84, 0x7e800000, v84
	v_mfma_f32_16x16x32_bf16 v[206:209], v[132:135], v[40:43], v[206:209]
	ds_read_b128 v[120:123], v95
	ds_read_b128 v[124:127], v95 offset:8192
	v_fmaak_f32 v78, v178, v77, 0x43000000
	v_fmaak_f32 v85, v186, v84, 0x43000000
	v_mfma_f32_16x16x32_bf16 v[194:197], v[136:139], v[12:15], v[194:197]
	v_cvt_pk_u8_f32 v80, v78, 0, 0
	v_cvt_pk_u8_f32 v82, v85, 0, 0
	v_mfma_f32_16x16x32_bf16 v[198:201], v[140:143], v[12:15], v[198:201]
	v_fmaak_f32 v78, v179, v77, 0x43000000
	v_fmaak_f32 v85, v187, v84, 0x43000000
	v_mfma_f32_16x16x32_bf16 v[202:205], v[136:139], v[44:47], v[202:205]
	v_cvt_pk_u8_f32 v80, v78, 1, v80
	v_cvt_pk_u8_f32 v82, v85, 1, v82
	v_mfma_f32_16x16x32_bf16 v[206:209], v[140:143], v[44:47], v[206:209]
	ds_read_b128 v[128:131], v96
	ds_read_b128 v[132:135], v96 offset:8192
	v_fmaak_f32 v78, v180, v77, 0x43000000
	v_fmaak_f32 v85, v188, v84, 0x43000000
	v_mfma_f32_16x16x32_bf16 v[194:197], v[144:147], v[16:19], v[194:197]
	v_cvt_pk_u8_f32 v80, v78, 2, v80
	v_cvt_pk_u8_f32 v82, v85, 2, v82
	v_mfma_f32_16x16x32_bf16 v[198:201], v[148:151], v[16:19], v[198:201]
	v_fmaak_f32 v78, v181, v77, 0x43000000
	v_fmaak_f32 v85, v189, v84, 0x43000000
	v_mfma_f32_16x16x32_bf16 v[202:205], v[144:147], v[48:51], v[202:205]
	v_cvt_pk_u8_f32 v80, v78, 3, v80
	v_cvt_pk_u8_f32 v82, v85, 3, v82
	v_mfma_f32_16x16x32_bf16 v[206:209], v[148:151], v[48:51], v[206:209]
	ds_read_b128 v[136:139], v97
	ds_read_b128 v[140:143], v97 offset:8192
	v_fmaak_f32 v78, v182, v77, 0x43000000
	v_fmaak_f32 v85, v190, v84, 0x43000000
	v_mfma_f32_16x16x32_bf16 v[194:197], v[152:155], v[20:23], v[194:197]
	v_cvt_pk_u8_f32 v81, v78, 0, 0
	v_cvt_pk_u8_f32 v83, v85, 0, 0
	v_mfma_f32_16x16x32_bf16 v[198:201], v[156:159], v[20:23], v[198:201]
	v_fmaak_f32 v78, v183, v77, 0x43000000
	v_fmaak_f32 v85, v191, v84, 0x43000000
	v_mfma_f32_16x16x32_bf16 v[202:205], v[152:155], v[52:55], v[202:205]
	v_cvt_pk_u8_f32 v81, v78, 1, v81
	v_cvt_pk_u8_f32 v83, v85, 1, v83
	v_mfma_f32_16x16x32_bf16 v[206:209], v[156:159], v[52:55], v[206:209]
	ds_read_b128 v[144:147], v98
	ds_read_b128 v[148:151], v98 offset:8192
	v_fmaak_f32 v78, v184, v77, 0x43000000
	v_fmaak_f32 v85, v192, v84, 0x43000000
	v_mfma_f32_16x16x32_bf16 v[194:197], v[160:163], v[24:27], v[194:197]
	v_cvt_pk_u8_f32 v81, v78, 2, v81
	v_cvt_pk_u8_f32 v83, v85, 2, v83
	v_mfma_f32_16x16x32_bf16 v[198:201], v[164:167], v[24:27], v[198:201]
	v_fmaak_f32 v78, v185, v77, 0x43000000
	v_fmaak_f32 v85, v193, v84, 0x43000000
	v_mfma_f32_16x16x32_bf16 v[202:205], v[160:163], v[56:59], v[202:205]
	v_cvt_pk_u8_f32 v81, v78, 3, v81
	v_cvt_pk_u8_f32 v83, v85, 3, v83
	v_mfma_f32_16x16x32_bf16 v[206:209], v[164:167], v[56:59], v[206:209]
	ds_read_b128 v[152:155], v99
	ds_read_b128 v[156:159], v99 offset:8192
	v_add_u16_e32 v79, 1, v79
	v_add_u16_e32 v110, 1, v110
	v_mfma_f32_16x16x32_bf16 v[194:197], v[168:171], v[28:31], v[194:197]
	ds_write_b8 v106, v79 offset:136
	ds_write_b8 v106, v110 offset:2696
	v_mfma_f32_16x16x32_bf16 v[198:201], v[172:175], v[28:31], v[198:201]
	ds_write2st64_b64 v108, v[80:81], v[82:83] offset1:5
	v_mfma_f32_16x16x32_bf16 v[202:205], v[168:171], v[60:63], v[202:205]
	v_mfma_f32_16x16x32_bf16 v[206:209], v[172:175], v[60:63], v[206:209]
	s_sub_i32 s36, s36, 1
	s_cmp_lg_u32 s36, 0
	s_cbranch_scc1 .Ldown_mid
	s_waitcnt vmcnt(2) lgkmcnt(0)
	s_barrier
; DI void phase_edown3(const Ctx& c, int layer) {
;     ...
;         D2_BODY(0, 0, 0); D2_BODY(1, 1, 0);
; #pragma unroll 1
;         for (int J = 2; J < 16; J += 2) { D2_BODY(0, J, 5); D2_BODY(1, J + 1, 0); }
	s_add_i32 m0, s30, 0xc000
	s_nop 0
	global_load_lds_dwordx4 v176, s[16:17]
	s_add_i32 m0, s30, 0xe000
	s_nop 0
	global_load_lds_dwordx4 v64, s[16:17]
	s_add_u32 s16, s16, 0x4000
	s_addc_u32 s17, s17, 0
	v_mfma_f32_16x16x32_bf16 v[178:181], v[112:115], v[0:3], 0
	v_mfma_f32_16x16x32_bf16 v[182:185], v[116:119], v[0:3], 0
	ds_read_b128 v[160:163], v100 offset:16384
	ds_read_b128 v[164:167], v100 offset:24576
	v_mfma_f32_16x16x32_bf16 v[186:189], v[112:115], v[32:35], 0
	v_mfma_f32_16x16x32_bf16 v[190:193], v[116:119], v[32:35], 0
	ds_read_b128 v[168:171], v101 offset:16384
	ds_read_b128 v[172:175], v101 offset:24576
	v_max3_f32 v77, |v194|, |v195|, |v196|
	v_max3_f32 v84, |v202|, |v203|, |v204|
	v_mfma_f32_16x16x32_bf16 v[178:181], v[120:123], v[4:7], v[178:181]
	v_max3_f32 v78, |v197|, |v198|, |v199|
	v_max3_f32 v85, |v205|, |v206|, |v207|
	v_mfma_f32_16x16x32_bf16 v[182:185], v[124:127], v[4:7], v[182:185]
	v_max3_f32 v77, |v200|, |v201|, v77
	v_max3_f32 v84, |v208|, |v209|, v84
	v_mfma_f32_16x16x32_bf16 v[186:189], v[120:123], v[36:39], v[186:189]
	v_max_f32_e32 v77, v77, v78
	v_max_f32_e32 v84, v84, v85
	v_mfma_f32_16x16x32_bf16 v[190:193], v[124:127], v[36:39], v[190:193]
	ds_read_b128 v[112:115], v94 offset:16384
	ds_read_b128 v[116:119], v94 offset:24576
	v_mul_f32_e32 v77, 0x3c010204, v77
	v_mul_f32_e32 v84, 0x3c010204, v84
	v_mfma_f32_16x16x32_bf16 v[178:181], v[128:131], v[8:11], v[178:181]
	v_lshrrev_b32_e32 v79, 23, v77
	v_lshrrev_b32_e32 v110, 23, v84
	v_mfma_f32_16x16x32_bf16 v[182:185], v[132:135], v[8:11], v[182:185]
	v_and_b32_e32 v77, 0x7f800000, v77
	v_and_b32_e32 v84, 0x7f800000, v84
	v_mfma_f32_16x16x32_bf16 v[186:189], v[128:131], v[40:43], v[186:189]
	v_sub_u32_e32 v77, 0x7e800000, v77
	v_sub_u32_e32 v84, 0x7e800000, v84
	v_mfma_f32_16x16x32_bf16 v[190:193], v[132:135], v[40:43], v[190:193]
	ds_read_b128 v[120:123], v95 offset:16384
	ds_read_b128 v[124:127], v95 offset:24576
	v_fmaak_f32 v78, v194, v77, 0x43000000
	v_fmaak_f32 v85, v202, v84, 0x43000000
	v_mfma_f32_16x16x32_bf16 v[178:181], v[136:139], v[12:15], v[178:181]
	v_cvt_pk_u8_f32 v80, v78, 0, 0
	v_cvt_pk_u8_f32 v82, v85, 0, 0
	v_mfma_f32_16x16x32_bf16 v[182:185], v[140:143], v[12:15], v[182:185]
	v_fmaak_f32 v78, v195, v77, 0x43000000
	v_fmaak_f32 v85, v203, v84, 0x43000000
	v_mfma_f32_16x16x32_bf16 v[186:189], v[136:139], v[44:47], v[186:189]
	v_cvt_pk_u8_f32 v80, v78, 1, v80
	v_cvt_pk_u8_f32 v82, v85, 1, v82
	v_mfma_f32_16x16x32_bf16 v[190:193], v[140:143], v[44:47], v[190:193]
	ds_read_b128 v[128:131], v96 offset:16384
	ds_read_b128 v[132:135], v96 offset:24576
	v_fmaak_f32 v78, v196, v77, 0x43000000
	v_fmaak_f32 v85, v204, v84, 0x43000000
	v_mfma_f32_16x16x32_bf16 v[178:181], v[144:147], v[16:19], v[178:181]
	v_cvt_pk_u8_f32 v80, v78, 2, v80
	v_cvt_pk_u8_f32 v82, v85, 2, v82
	v_mfma_f32_16x16x32_bf16 v[182:185], v[148:151], v[16:19], v[182:185]
	v_fmaak_f32 v78, v197, v77, 0x43000000
	v_fmaak_f32 v85, v205, v84, 0x43000000
	v_mfma_f32_16x16x32_bf16 v[186:189], v[144:147], v[48:51], v[186:189]
	v_cvt_pk_u8_f32 v80, v78, 3, v80
	v_cvt_pk_u8_f32 v82, v85, 3, v82
	v_mfma_f32_16x16x32_bf16 v[190:193], v[148:151], v[48:51], v[190:193]
	ds_read_b128 v[136:139], v97 offset:16384
	ds_read_b128 v[140:143], v97 offset:24576
	v_fmaak_f32 v78, v198, v77, 0x43000000
	v_fmaak_f32 v85, v206, v84, 0x43000000
	v_mfma_f32_16x16x32_bf16 v[178:181], v[152:155], v[20:23], v[178:181]
	v_cvt_pk_u8_f32 v81, v78, 0, 0
	v_cvt_pk_u8_f32 v83, v85, 0, 0
	v_mfma_f32_16x16x32_bf16 v[182:185], v[156:159], v[20:23], v[182:185]
	v_fmaak_f32 v78, v199, v77, 0x43000000
	v_fmaak_f32 v85, v207, v84, 0x43000000
	v_mfma_f32_16x16x32_bf16 v[186:189], v[152:155], v[52:55], v[186:189]
	v_cvt_pk_u8_f32 v81, v78, 1, v81
	v_cvt_pk_u8_f32 v83, v85, 1, v83
	v_mfma_f32_16x16x32_bf16 v[190:193], v[156:159], v[52:55], v[190:193]
	ds_read_b128 v[144:147], v98 offset:16384
	ds_read_b128 v[148:151], v98 offset:24576
	v_fmaak_f32 v78, v200, v77, 0x43000000
	v_fmaak_f32 v85, v208, v84, 0x43000000
	v_mfma_f32_16x16x32_bf16 v[178:181], v[210:213], v[24:27], v[178:181]
	v_cvt_pk_u8_f32 v81, v78, 2, v81
	v_cvt_pk_u8_f32 v83, v85, 2, v83
	v_mfma_f32_16x16x32_bf16 v[182:185], v[214:217], v[24:27], v[182:185]
	v_fmaak_f32 v78, v201, v77, 0x43000000
	v_fmaak_f32 v85, v209, v84, 0x43000000
	v_mfma_f32_16x16x32_bf16 v[186:189], v[210:213], v[56:59], v[186:189]
	v_cvt_pk_u8_f32 v81, v78, 3, v81
	v_cvt_pk_u8_f32 v83, v85, 3, v83
	v_mfma_f32_16x16x32_bf16 v[190:193], v[214:217], v[56:59], v[190:193]
	ds_read_b128 v[152:155], v99 offset:16384
	ds_read_b128 v[156:159], v99 offset:24576
	v_add_u16_e32 v79, 1, v79
	v_add_u16_e32 v110, 1, v110
	v_mfma_f32_16x16x32_bf16 v[178:181], v[236:239], v[28:31], v[178:181]
	ds_write_b8 v106, v79 offset:140
	ds_write_b8 v106, v110 offset:2700
	v_mfma_f32_16x16x32_bf16 v[182:185], v[240:243], v[28:31], v[182:185]
	ds_write2st64_b64 v109, v[80:81], v[82:83] offset1:5
	v_mfma_f32_16x16x32_bf16 v[186:189], v[236:239], v[60:63], v[186:189]
	v_mfma_f32_16x16x32_bf16 v[190:193], v[240:243], v[60:63], v[190:193]
	s_waitcnt lgkmcnt(0)
	ds_read_b128 v[194:197], v103
	ds_read_b128 v[198:201], v103 offset:1280
	ds_read_b128 v[202:205], v103 offset:2560
	ds_read_b128 v[206:209], v103 offset:3840
	ds_read_b128 v[244:247], v104 offset:128
	s_waitcnt vmcnt(2) lgkmcnt(0)
	s_barrier
; DI void phase_edown3(const Ctx& c, int layer) {
;     ...
;         D2_BODY(0, 0, 0); D2_BODY(1, 1, 0);
; #pragma unroll 1
;         for (int J = 2; J < 16; J += 2) { D2_BODY(0, J, 5); D2_BODY(1, J + 1, 0); }
	global_store_dwordx4 v72, v[194:197], s[10:11] nt
	global_store_dwordx4 v73, v[198:201], s[10:11] nt
	global_store_dwordx4 v74, v[202:205], s[10:11] nt
	global_store_dwordx4 v75, v[206:209], s[10:11] nt
	s_and_saveexec_b64 s[8:9], s[2:3]
	global_store_dwordx4 v76, v[244:247], s[10:11] nt
	s_or_b64 exec, exec, s[8:9]
	v_add_u32_e32 v72, 0x80, v72
	v_add_u32_e32 v73, 0x80, v73
	v_add_u32_e32 v74, 0x80, v74
	v_add_u32_e32 v75, 0x80, v75
	v_add_u32_e32 v76, 16, v76
	v_mfma_f32_16x16x32_bf16 v[194:197], v[112:115], v[0:3], 0
	v_mfma_f32_16x16x32_bf16 v[198:201], v[116:119], v[0:3], 0
	ds_read_b128 v[210:213], v100 offset:32768
	ds_read_b128 v[214:217], v100 offset:40960
	v_mfma_f32_16x16x32_bf16 v[202:205], v[112:115], v[32:35], 0
	v_mfma_f32_16x16x32_bf16 v[206:209], v[116:119], v[32:35], 0
	ds_read_b128 v[236:239], v101 offset:32768
	ds_read_b128 v[240:243], v101 offset:40960
	v_max3_f32 v77, |v178|, |v179|, |v180|
	v_max3_f32 v84, |v186|, |v187|, |v188|
	v_mfma_f32_16x16x32_bf16 v[194:197], v[120:123], v[4:7], v[194:197]
	v_max3_f32 v78, |v181|, |v182|, |v183|
	v_max3_f32 v85, |v189|, |v190|, |v191|
	v_mfma_f32_16x16x32_bf16 v[198:201], v[124:127], v[4:7], v[198:201]
	v_max3_f32 v77, |v184|, |v185|, v77
	v_max3_f32 v84, |v192|, |v193|, v84
	v_mfma_f32_16x16x32_bf16 v[202:205], v[120:123], v[36:39], v[202:205]
	v_max_f32_e32 v77, v77, v78
	v_max_f32_e32 v84, v84, v85
	v_mfma_f32_16x16x32_bf16 v[206:209], v[124:127], v[36:39], v[206:209]
	ds_read_b128 v[112:115], v94 offset:32768
	ds_read_b128 v[116:119], v94 offset:40960
	v_mul_f32_e32 v77, 0x3c010204, v77
	v_mul_f32_e32 v84, 0x3c010204, v84
	v_mfma_f32_16x16x32_bf16 v[194:197], v[128:131], v[8:11], v[194:197]
	v_lshrrev_b32_e32 v79, 23, v77
	v_lshrrev_b32_e32 v110, 23, v84
	v_mfma_f32_16x16x32_bf16 v[198:201], v[132:135], v[8:11], v[198:201]
	v_and_b32_e32 v77, 0x7f800000, v77
	v_and_b32_e32 v84, 0x7f800000, v84
	v_mfma_f32_16x16x32_bf16 v[202:205], v[128:131], v[40:43], v[202:205]
	v_sub_u32_e32 v77, 0x7e800000, v77
	v_sub_u32_e32 v84, 0x7e800000, v84
	v_mfma_f32_16x16x32_bf16 v[206:209], v[132:135], v[40:43], v[206:209]
	ds_read_b128 v[120:123], v95 offset:32768
	ds_read_b128 v[124:127], v95 offset:40960
	v_fmaak_f32 v78, v178, v77, 0x43000000
	v_fmaak_f32 v85, v186, v84, 0x43000000
	v_mfma_f32_16x16x32_bf16 v[194:197], v[136:139], v[12:15], v[194:197]
	v_cvt_pk_u8_f32 v80, v78, 0, 0
	v_cvt_pk_u8_f32 v82, v85, 0, 0
	v_mfma_f32_16x16x32_bf16 v[198:201], v[140:143], v[12:15], v[198:201]
	v_fmaak_f32 v78, v179, v77, 0x43000000
	v_fmaak_f32 v85, v187, v84, 0x43000000
	v_mfma_f32_16x16x32_bf16 v[202:205], v[136:139], v[44:47], v[202:205]
	v_cvt_pk_u8_f32 v80, v78, 1, v80
	v_cvt_pk_u8_f32 v82, v85, 1, v82
	v_mfma_f32_16x16x32_bf16 v[206:209], v[140:143], v[44:47], v[206:209]
	ds_read_b128 v[128:131], v96 offset:32768
	ds_read_b128 v[132:135], v96 offset:40960
	v_fmaak_f32 v78, v180, v77, 0x43000000
	v_fmaak_f32 v85, v188, v84, 0x43000000
	v_mfma_f32_16x16x32_bf16 v[194:197], v[144:147], v[16:19], v[194:197]
	v_cvt_pk_u8_f32 v80, v78, 2, v80
	v_cvt_pk_u8_f32 v82, v85, 2, v82
	v_mfma_f32_16x16x32_bf16 v[198:201], v[148:151], v[16:19], v[198:201]
	v_fmaak_f32 v78, v181, v77, 0x43000000
	v_fmaak_f32 v85, v189, v84, 0x43000000
	v_mfma_f32_16x16x32_bf16 v[202:205], v[144:147], v[48:51], v[202:205]
	v_cvt_pk_u8_f32 v80, v78, 3, v80
	v_cvt_pk_u8_f32 v82, v85, 3, v82
	v_mfma_f32_16x16x32_bf16 v[206:209], v[148:151], v[48:51], v[206:209]
	ds_read_b128 v[136:139], v97 offset:32768
	ds_read_b128 v[140:143], v97 offset:40960
	v_fmaak_f32 v78, v182, v77, 0x43000000
	v_fmaak_f32 v85, v190, v84, 0x43000000
	v_mfma_f32_16x16x32_bf16 v[194:197], v[152:155], v[20:23], v[194:197]
	v_cvt_pk_u8_f32 v81, v78, 0, 0
	v_cvt_pk_u8_f32 v83, v85, 0, 0
	v_mfma_f32_16x16x32_bf16 v[198:201], v[156:159], v[20:23], v[198:201]
	v_fmaak_f32 v78, v183, v77, 0x43000000
	v_fmaak_f32 v85, v191, v84, 0x43000000
	v_mfma_f32_16x16x32_bf16 v[202:205], v[152:155], v[52:55], v[202:205]
	v_cvt_pk_u8_f32 v81, v78, 1, v81
	v_cvt_pk_u8_f32 v83, v85, 1, v83
	v_mfma_f32_16x16x32_bf16 v[206:209], v[156:159], v[52:55], v[206:209]
	ds_read_b128 v[144:147], v98 offset:32768
	ds_read_b128 v[148:151], v98 offset:40960
	v_fmaak_f32 v78, v184, v77, 0x43000000
	v_fmaak_f32 v85, v192, v84, 0x43000000
	v_mfma_f32_16x16x32_bf16 v[194:197], v[160:163], v[24:27], v[194:197]
	v_cvt_pk_u8_f32 v81, v78, 2, v81
	v_cvt_pk_u8_f32 v83, v85, 2, v83
	v_mfma_f32_16x16x32_bf16 v[198:201], v[164:167], v[24:27], v[198:201]
	v_fmaak_f32 v78, v185, v77, 0x43000000
	v_fmaak_f32 v85, v193, v84, 0x43000000
	v_mfma_f32_16x16x32_bf16 v[202:205], v[160:163], v[56:59], v[202:205]
	v_cvt_pk_u8_f32 v81, v78, 3, v81
	v_cvt_pk_u8_f32 v83, v85, 3, v83
	v_mfma_f32_16x16x32_bf16 v[206:209], v[164:167], v[56:59], v[206:209]
	ds_read_b128 v[152:155], v99 offset:32768
	ds_read_b128 v[156:159], v99 offset:40960
	v_add_u16_e32 v79, 1, v79
	v_add_u16_e32 v110, 1, v110
	v_mfma_f32_16x16x32_bf16 v[194:197], v[168:171], v[28:31], v[194:197]
	ds_write_b8 v106, v79 offset:128
	ds_write_b8 v106, v110 offset:2688
	v_mfma_f32_16x16x32_bf16 v[198:201], v[172:175], v[28:31], v[198:201]
	ds_write2st64_b64 v102, v[80:81], v[82:83] offset1:5
	v_mfma_f32_16x16x32_bf16 v[202:205], v[168:171], v[60:63], v[202:205]
	v_mfma_f32_16x16x32_bf16 v[206:209], v[172:175], v[60:63], v[206:209]
	s_waitcnt vmcnt(5) lgkmcnt(0)
	s_barrier
; DI void phase_edown3(const Ctx& c, int layer) {
;     ...
;         D2_BODY(0, 0, 0); D2_BODY(1, 1, 0);
; #pragma unroll 1
;         for (int J = 2; J < 16; J += 2) { D2_BODY(0, J, 5); D2_BODY(1, J + 1, 0); }
	v_mfma_f32_16x16x32_bf16 v[178:181], v[112:115], v[0:3], 0
	v_mfma_f32_16x16x32_bf16 v[182:185], v[116:119], v[0:3], 0
	ds_read_b128 v[160:163], v100 offset:49152
	ds_read_b128 v[164:167], v100 offset:57344
	v_mfma_f32_16x16x32_bf16 v[186:189], v[112:115], v[32:35], 0
	v_mfma_f32_16x16x32_bf16 v[190:193], v[116:119], v[32:35], 0
	ds_read_b128 v[168:171], v101 offset:49152
	ds_read_b128 v[172:175], v101 offset:57344
	v_max3_f32 v77, |v194|, |v195|, |v196|
	v_max3_f32 v84, |v202|, |v203|, |v204|
	v_mfma_f32_16x16x32_bf16 v[178:181], v[120:123], v[4:7], v[178:181]
	v_max3_f32 v78, |v197|, |v198|, |v199|
	v_max3_f32 v85, |v205|, |v206|, |v207|
	v_mfma_f32_16x16x32_bf16 v[182:185], v[124:127], v[4:7], v[182:185]
	v_max3_f32 v77, |v200|, |v201|, v77
	v_max3_f32 v84, |v208|, |v209|, v84
	v_mfma_f32_16x16x32_bf16 v[186:189], v[120:123], v[36:39], v[186:189]
	v_max_f32_e32 v77, v77, v78
	v_max_f32_e32 v84, v84, v85
	v_mfma_f32_16x16x32_bf16 v[190:193], v[124:127], v[36:39], v[190:193]
	ds_read_b128 v[112:115], v94 offset:49152
	ds_read_b128 v[116:119], v94 offset:57344
	v_mul_f32_e32 v77, 0x3c010204, v77
	v_mul_f32_e32 v84, 0x3c010204, v84
	v_mfma_f32_16x16x32_bf16 v[178:181], v[128:131], v[8:11], v[178:181]
	v_lshrrev_b32_e32 v79, 23, v77
	v_lshrrev_b32_e32 v110, 23, v84
	v_mfma_f32_16x16x32_bf16 v[182:185], v[132:135], v[8:11], v[182:185]
	v_and_b32_e32 v77, 0x7f800000, v77
	v_and_b32_e32 v84, 0x7f800000, v84
	v_mfma_f32_16x16x32_bf16 v[186:189], v[128:131], v[40:43], v[186:189]
	v_sub_u32_e32 v77, 0x7e800000, v77
	v_sub_u32_e32 v84, 0x7e800000, v84
	v_mfma_f32_16x16x32_bf16 v[190:193], v[132:135], v[40:43], v[190:193]
	ds_read_b128 v[120:123], v95 offset:49152
	ds_read_b128 v[124:127], v95 offset:57344
	v_fmaak_f32 v78, v194, v77, 0x43000000
	v_fmaak_f32 v85, v202, v84, 0x43000000
	v_mfma_f32_16x16x32_bf16 v[178:181], v[136:139], v[12:15], v[178:181]
	v_cvt_pk_u8_f32 v80, v78, 0, 0
	v_cvt_pk_u8_f32 v82, v85, 0, 0
	v_mfma_f32_16x16x32_bf16 v[182:185], v[140:143], v[12:15], v[182:185]
	v_fmaak_f32 v78, v195, v77, 0x43000000
	v_fmaak_f32 v85, v203, v84, 0x43000000
	v_mfma_f32_16x16x32_bf16 v[186:189], v[136:139], v[44:47], v[186:189]
	v_cvt_pk_u8_f32 v80, v78, 1, v80
	v_cvt_pk_u8_f32 v82, v85, 1, v82
	v_mfma_f32_16x16x32_bf16 v[190:193], v[140:143], v[44:47], v[190:193]
	ds_read_b128 v[128:131], v96 offset:49152
	ds_read_b128 v[132:135], v96 offset:57344
	v_fmaak_f32 v78, v196, v77, 0x43000000
	v_fmaak_f32 v85, v204, v84, 0x43000000
	v_mfma_f32_16x16x32_bf16 v[178:181], v[144:147], v[16:19], v[178:181]
	v_cvt_pk_u8_f32 v80, v78, 2, v80
	v_cvt_pk_u8_f32 v82, v85, 2, v82
	v_mfma_f32_16x16x32_bf16 v[182:185], v[148:151], v[16:19], v[182:185]
	v_fmaak_f32 v78, v197, v77, 0x43000000
	v_fmaak_f32 v85, v205, v84, 0x43000000
	v_mfma_f32_16x16x32_bf16 v[186:189], v[144:147], v[48:51], v[186:189]
	v_cvt_pk_u8_f32 v80, v78, 3, v80
	v_cvt_pk_u8_f32 v82, v85, 3, v82
	v_mfma_f32_16x16x32_bf16 v[190:193], v[148:151], v[48:51], v[190:193]
	ds_read_b128 v[136:139], v97 offset:49152
	ds_read_b128 v[140:143], v97 offset:57344
	v_fmaak_f32 v78, v198, v77, 0x43000000
	v_fmaak_f32 v85, v206, v84, 0x43000000
	v_mfma_f32_16x16x32_bf16 v[178:181], v[152:155], v[20:23], v[178:181]
	v_cvt_pk_u8_f32 v81, v78, 0, 0
	v_cvt_pk_u8_f32 v83, v85, 0, 0
	v_mfma_f32_16x16x32_bf16 v[182:185], v[156:159], v[20:23], v[182:185]
	v_fmaak_f32 v78, v199, v77, 0x43000000
	v_fmaak_f32 v85, v207, v84, 0x43000000
	v_mfma_f32_16x16x32_bf16 v[186:189], v[152:155], v[52:55], v[186:189]
	v_cvt_pk_u8_f32 v81, v78, 1, v81
	v_cvt_pk_u8_f32 v83, v85, 1, v83
	v_mfma_f32_16x16x32_bf16 v[190:193], v[156:159], v[52:55], v[190:193]
	ds_read_b128 v[144:147], v98 offset:49152
	ds_read_b128 v[148:151], v98 offset:57344
	v_fmaak_f32 v78, v200, v77, 0x43000000
	v_fmaak_f32 v85, v208, v84, 0x43000000
	v_mfma_f32_16x16x32_bf16 v[178:181], v[210:213], v[24:27], v[178:181]
	v_cvt_pk_u8_f32 v81, v78, 2, v81
	v_cvt_pk_u8_f32 v83, v85, 2, v83
	v_mfma_f32_16x16x32_bf16 v[182:185], v[214:217], v[24:27], v[182:185]
	v_fmaak_f32 v78, v201, v77, 0x43000000
	v_fmaak_f32 v85, v209, v84, 0x43000000
	v_mfma_f32_16x16x32_bf16 v[186:189], v[210:213], v[56:59], v[186:189]
	v_cvt_pk_u8_f32 v81, v78, 3, v81
	v_cvt_pk_u8_f32 v83, v85, 3, v83
	v_mfma_f32_16x16x32_bf16 v[190:193], v[214:217], v[56:59], v[190:193]
	ds_read_b128 v[152:155], v99 offset:49152
	ds_read_b128 v[156:159], v99 offset:57344
	v_add_u16_e32 v79, 1, v79
	v_add_u16_e32 v110, 1, v110
	v_mfma_f32_16x16x32_bf16 v[178:181], v[236:239], v[28:31], v[178:181]
	ds_write_b8 v106, v79 offset:132
	ds_write_b8 v106, v110 offset:2692
	v_mfma_f32_16x16x32_bf16 v[182:185], v[240:243], v[28:31], v[182:185]
	ds_write2st64_b64 v107, v[80:81], v[82:83] offset1:5
	v_mfma_f32_16x16x32_bf16 v[186:189], v[236:239], v[60:63], v[186:189]
	v_mfma_f32_16x16x32_bf16 v[190:193], v[240:243], v[60:63], v[190:193]
	s_waitcnt lgkmcnt(0)
	s_barrier
; DI void phase_edown3(const Ctx& c, int layer) {
;     ...
;         D2_BODY(0, 0, 0); D2_BODY(1, 1, 0);
; #pragma unroll 1
;         for (int J = 2; J < 16; J += 2) { D2_BODY(0, J, 5); D2_BODY(1, J + 1, 0); }
	v_mfma_f32_16x16x32_bf16 v[194:197], v[112:115], v[0:3], 0
	v_mfma_f32_16x16x32_bf16 v[198:201], v[116:119], v[0:3], 0
	v_mfma_f32_16x16x32_bf16 v[202:205], v[112:115], v[32:35], 0
	v_mfma_f32_16x16x32_bf16 v[206:209], v[116:119], v[32:35], 0
	v_max3_f32 v77, |v178|, |v179|, |v180|
	v_max3_f32 v84, |v186|, |v187|, |v188|
	v_mfma_f32_16x16x32_bf16 v[194:197], v[120:123], v[4:7], v[194:197]
	v_max3_f32 v78, |v181|, |v182|, |v183|
	v_max3_f32 v85, |v189|, |v190|, |v191|
	v_mfma_f32_16x16x32_bf16 v[198:201], v[124:127], v[4:7], v[198:201]
	v_max3_f32 v77, |v184|, |v185|, v77
	v_max3_f32 v84, |v192|, |v193|, v84
	v_mfma_f32_16x16x32_bf16 v[202:205], v[120:123], v[36:39], v[202:205]
	v_max_f32_e32 v77, v77, v78
	v_max_f32_e32 v84, v84, v85
	v_mfma_f32_16x16x32_bf16 v[206:209], v[124:127], v[36:39], v[206:209]
	v_mul_f32_e32 v77, 0x3c010204, v77
	v_mul_f32_e32 v84, 0x3c010204, v84
	v_mfma_f32_16x16x32_bf16 v[194:197], v[128:131], v[8:11], v[194:197]
	v_lshrrev_b32_e32 v79, 23, v77
	v_lshrrev_b32_e32 v110, 23, v84
	v_mfma_f32_16x16x32_bf16 v[198:201], v[132:135], v[8:11], v[198:201]
	v_and_b32_e32 v77, 0x7f800000, v77
	v_and_b32_e32 v84, 0x7f800000, v84
	v_mfma_f32_16x16x32_bf16 v[202:205], v[128:131], v[40:43], v[202:205]
	v_sub_u32_e32 v77, 0x7e800000, v77
	v_sub_u32_e32 v84, 0x7e800000, v84
	v_mfma_f32_16x16x32_bf16 v[206:209], v[132:135], v[40:43], v[206:209]
	v_fmaak_f32 v78, v178, v77, 0x43000000
	v_fmaak_f32 v85, v186, v84, 0x43000000
	v_mfma_f32_16x16x32_bf16 v[194:197], v[136:139], v[12:15], v[194:197]
	v_cvt_pk_u8_f32 v80, v78, 0, 0
	v_cvt_pk_u8_f32 v82, v85, 0, 0
	v_mfma_f32_16x16x32_bf16 v[198:201], v[140:143], v[12:15], v[198:201]
	v_fmaak_f32 v78, v179, v77, 0x43000000
	v_fmaak_f32 v85, v187, v84, 0x43000000
	v_mfma_f32_16x16x32_bf16 v[202:205], v[136:139], v[44:47], v[202:205]
	v_cvt_pk_u8_f32 v80, v78, 1, v80
	v_cvt_pk_u8_f32 v82, v85, 1, v82
	v_mfma_f32_16x16x32_bf16 v[206:209], v[140:143], v[44:47], v[206:209]
	v_fmaak_f32 v78, v180, v77, 0x43000000
	v_fmaak_f32 v85, v188, v84, 0x43000000
	v_mfma_f32_16x16x32_bf16 v[194:197], v[144:147], v[16:19], v[194:197]
	v_cvt_pk_u8_f32 v80, v78, 2, v80
	v_cvt_pk_u8_f32 v82, v85, 2, v82
	v_mfma_f32_16x16x32_bf16 v[198:201], v[148:151], v[16:19], v[198:201]
	v_fmaak_f32 v78, v181, v77, 0x43000000
	v_fmaak_f32 v85, v189, v84, 0x43000000
	v_mfma_f32_16x16x32_bf16 v[202:205], v[144:147], v[48:51], v[202:205]
	v_cvt_pk_u8_f32 v80, v78, 3, v80
	v_cvt_pk_u8_f32 v82, v85, 3, v82
	v_mfma_f32_16x16x32_bf16 v[206:209], v[148:151], v[48:51], v[206:209]
	v_fmaak_f32 v78, v182, v77, 0x43000000
	v_fmaak_f32 v85, v190, v84, 0x43000000
	v_mfma_f32_16x16x32_bf16 v[194:197], v[152:155], v[20:23], v[194:197]
	v_cvt_pk_u8_f32 v81, v78, 0, 0
	v_cvt_pk_u8_f32 v83, v85, 0, 0
	v_mfma_f32_16x16x32_bf16 v[198:201], v[156:159], v[20:23], v[198:201]
	v_fmaak_f32 v78, v183, v77, 0x43000000
	v_fmaak_f32 v85, v191, v84, 0x43000000
	v_mfma_f32_16x16x32_bf16 v[202:205], v[152:155], v[52:55], v[202:205]
	v_cvt_pk_u8_f32 v81, v78, 1, v81
	v_cvt_pk_u8_f32 v83, v85, 1, v83
	v_mfma_f32_16x16x32_bf16 v[206:209], v[156:159], v[52:55], v[206:209]
	v_fmaak_f32 v78, v184, v77, 0x43000000
	v_fmaak_f32 v85, v192, v84, 0x43000000
	v_mfma_f32_16x16x32_bf16 v[194:197], v[160:163], v[24:27], v[194:197]
	v_cvt_pk_u8_f32 v81, v78, 2, v81
	v_cvt_pk_u8_f32 v83, v85, 2, v83
	v_mfma_f32_16x16x32_bf16 v[198:201], v[164:167], v[24:27], v[198:201]
	v_fmaak_f32 v78, v185, v77, 0x43000000
	v_fmaak_f32 v85, v193, v84, 0x43000000
	v_mfma_f32_16x16x32_bf16 v[202:205], v[160:163], v[56:59], v[202:205]
	v_cvt_pk_u8_f32 v81, v78, 3, v81
	v_cvt_pk_u8_f32 v83, v85, 3, v83
	v_mfma_f32_16x16x32_bf16 v[206:209], v[164:167], v[56:59], v[206:209]
	v_add_u16_e32 v79, 1, v79
	v_add_u16_e32 v110, 1, v110
	v_mfma_f32_16x16x32_bf16 v[194:197], v[168:171], v[28:31], v[194:197]
	ds_write_b8 v106, v79 offset:136
	ds_write_b8 v106, v110 offset:2696
	v_mfma_f32_16x16x32_bf16 v[198:201], v[172:175], v[28:31], v[198:201]
	ds_write2st64_b64 v108, v[80:81], v[82:83] offset1:5
	v_mfma_f32_16x16x32_bf16 v[202:205], v[168:171], v[60:63], v[202:205]
	v_mfma_f32_16x16x32_bf16 v[206:209], v[172:175], v[60:63], v[206:209]
	s_nop 7
	v_max3_f32 v77, |v194|, |v195|, |v196|
	v_max3_f32 v84, |v202|, |v203|, |v204|
	v_max3_f32 v78, |v197|, |v198|, |v199|
	v_max3_f32 v85, |v205|, |v206|, |v207|
	v_max3_f32 v77, |v200|, |v201|, v77
	v_max3_f32 v84, |v208|, |v209|, v84
	v_max_f32_e32 v77, v77, v78
	v_max_f32_e32 v84, v84, v85
	v_mul_f32_e32 v77, 0x3c010204, v77
	v_mul_f32_e32 v84, 0x3c010204, v84
	v_lshrrev_b32_e32 v79, 23, v77
	v_lshrrev_b32_e32 v110, 23, v84
	v_and_b32_e32 v77, 0x7f800000, v77
	v_and_b32_e32 v84, 0x7f800000, v84
	v_sub_u32_e32 v77, 0x7e800000, v77
	v_sub_u32_e32 v84, 0x7e800000, v84
	v_fmaak_f32 v78, v194, v77, 0x43000000
	v_fmaak_f32 v85, v202, v84, 0x43000000
	v_cvt_pk_u8_f32 v80, v78, 0, 0
	v_cvt_pk_u8_f32 v82, v85, 0, 0
	v_fmaak_f32 v78, v195, v77, 0x43000000
	v_fmaak_f32 v85, v203, v84, 0x43000000
	v_cvt_pk_u8_f32 v80, v78, 1, v80
	v_cvt_pk_u8_f32 v82, v85, 1, v82
	v_fmaak_f32 v78, v196, v77, 0x43000000
	v_fmaak_f32 v85, v204, v84, 0x43000000
	v_cvt_pk_u8_f32 v80, v78, 2, v80
	v_cvt_pk_u8_f32 v82, v85, 2, v82
	v_fmaak_f32 v78, v197, v77, 0x43000000
	v_fmaak_f32 v85, v205, v84, 0x43000000
	v_cvt_pk_u8_f32 v80, v78, 3, v80
	v_cvt_pk_u8_f32 v82, v85, 3, v82
	v_fmaak_f32 v78, v198, v77, 0x43000000
	v_fmaak_f32 v85, v206, v84, 0x43000000
	v_cvt_pk_u8_f32 v81, v78, 0, 0
	v_cvt_pk_u8_f32 v83, v85, 0, 0
	v_fmaak_f32 v78, v199, v77, 0x43000000
	v_fmaak_f32 v85, v207, v84, 0x43000000
	v_cvt_pk_u8_f32 v81, v78, 1, v81
	v_cvt_pk_u8_f32 v83, v85, 1, v83
	v_fmaak_f32 v78, v200, v77, 0x43000000
	v_fmaak_f32 v85, v208, v84, 0x43000000
	v_cvt_pk_u8_f32 v81, v78, 2, v81
	v_cvt_pk_u8_f32 v83, v85, 2, v83
	v_fmaak_f32 v78, v201, v77, 0x43000000
	v_fmaak_f32 v85, v209, v84, 0x43000000
	v_cvt_pk_u8_f32 v81, v78, 3, v81
	v_cvt_pk_u8_f32 v83, v85, 3, v83
	v_add_u16_e32 v79, 1, v79
	v_add_u16_e32 v110, 1, v110
	ds_write_b8 v106, v79 offset:140
	ds_write_b8 v106, v110 offset:2700
	ds_write2st64_b64 v109, v[80:81], v[82:83] offset1:5
	s_waitcnt lgkmcnt(0)
	ds_read_b128 v[178:181], v103
	ds_read_b128 v[182:185], v103 offset:1280
	ds_read_b128 v[186:189], v103 offset:2560
	ds_read_b128 v[190:193], v103 offset:3840
	ds_read_b128 v[244:247], v104 offset:128
	s_waitcnt lgkmcnt(0)
	global_store_dwordx4 v72, v[178:181], s[10:11] nt
	global_store_dwordx4 v73, v[182:185], s[10:11] nt
	global_store_dwordx4 v74, v[186:189], s[10:11] nt
	global_store_dwordx4 v75, v[190:193], s[10:11] nt
	s_and_saveexec_b64 s[8:9], s[2:3]
	global_store_dwordx4 v76, v[244:247], s[10:11] nt
	s_or_b64 exec, exec, s[8:9]
	v_add_u32_e32 v72, 0x80, v72
	v_add_u32_e32 v73, 0x80, v73
	v_add_u32_e32 v74, 0x80, v74
	v_add_u32_e32 v75, 0x80, v75
	v_add_u32_e32 v76, 16, v76
	s_branch .LBB0_1256
